# v50 + route phase: the 16 loads of a wave's 8-row copy to the expert rows issued together up front; each row's stores wait only for their own loads
# speedup vs baseline: 1.0034x; 1.0034x over previous
; #define GAS __attribute__((address_space(1)))
; #define LAS __attribute__((address_space(3)))
; #define VM_WAIT() asm volatile("s_waitcnt vmcnt(0)" ::: "memory")
; __device__ __forceinline__ void route_phase(Frame& F) {
;     ...
;         VM_WAIT();
;         { unsigned char* XGS = F.ws + WS_XGS;
; #pragma unroll
;           for (int i = 0; i < 8; ++i) { const int row = base + F.wave * 8 + i; const LAS int* pr = lrow + (F.wave * 8 + i) * 4;
;               const v4u* src = (const v4u*)((const unsigned char*)XN + (size_t)row * DM) + F.lane;
;               const v4u x0 = __builtin_nontemporal_load((const GAS v4u*)src), x1 = __builtin_nontemporal_load((const GAS v4u*)(src + 64));
; #pragma unroll
;               for (int sl = 0; sl < 2; ++sl) { const int e = pr[2 * sl], rk = lbase[e] + pr[2 * sl + 1];
;                   GAS v4u* dst = (GAS v4u*)(XGS + ((size_t)e * ML + rk) * DM) + F.lane; dst[0] = x0; dst[64] = x1; } } }
.LBB0_1741:
	s_or_b64 exec, exec, s[0:1]
	s_ashr_i32 s27, s26, 31
	s_lshl_b64 s[0:1], s[26:27], 11
	s_waitcnt vmcnt(0)
	v_lshl_add_u64 v[2:3], v[32:33], 0, s[0:1]
	v_mov_b32_e32 v220, v2
	v_mov_b32_e32 v221, v3
	s_mov_b64 s[98:99], 0x800
	v_lshl_add_u64 v[222:223], v[2:3], 0, s[98:99]
	s_mov_b64 s[98:99], 0x1000
	v_lshl_add_u64 v[224:225], v[2:3], 0, s[98:99]
	s_mov_b64 s[98:99], 0x1800
	v_lshl_add_u64 v[226:227], v[2:3], 0, s[98:99]
	s_mov_b64 s[98:99], 0x2000
	v_lshl_add_u64 v[228:229], v[2:3], 0, s[98:99]
	s_mov_b64 s[98:99], 0x2800
	v_lshl_add_u64 v[230:231], v[2:3], 0, s[98:99]
	s_mov_b64 s[98:99], 0x3000
	v_lshl_add_u64 v[232:233], v[2:3], 0, s[98:99]
	s_mov_b64 s[98:99], 0x3800
	v_lshl_add_u64 v[234:235], v[2:3], 0, s[98:99]
	global_load_dwordx4 v[150:153], v[220:221], off nt
	global_load_dwordx4 v[154:157], v[220:221], off offset:1024 nt
	global_load_dwordx4 v[158:161], v[222:223], off nt
	global_load_dwordx4 v[162:165], v[222:223], off offset:1024 nt
	global_load_dwordx4 v[166:169], v[224:225], off nt
	global_load_dwordx4 v[170:173], v[224:225], off offset:1024 nt
	global_load_dwordx4 v[174:177], v[226:227], off nt
	global_load_dwordx4 v[182:185], v[226:227], off offset:1024 nt
	global_load_dwordx4 v[186:189], v[228:229], off nt
	global_load_dwordx4 v[190:193], v[228:229], off offset:1024 nt
	global_load_dwordx4 v[194:197], v[230:231], off nt
	global_load_dwordx4 v[200:203], v[230:231], off offset:1024 nt
	global_load_dwordx4 v[204:207], v[232:233], off nt
	global_load_dwordx4 v[208:211], v[232:233], off offset:1024 nt
	global_load_dwordx4 v[212:215], v[234:235], off nt
	global_load_dwordx4 v[216:219], v[234:235], off offset:1024 nt
	v_mov_b32_e32 v2, s45
	ds_read_b128 v[12:15], v2 offset:64
	ds_read_b128 v[16:19], v2 offset:80
	s_or_b32 s0, s26, 1
	s_ashr_i32 s1, s0, 31
	s_lshl_b64 s[0:1], s[0:1], 11
	s_waitcnt lgkmcnt(1)
	v_lshlrev_b32_e32 v3, 2, v12
	v_ashrrev_i32_e32 v57, 31, v12
	v_mov_b32_e32 v56, v12
	v_lshlrev_b32_e32 v12, 2, v14
	v_add_u32_e32 v3, 0, v3
	v_add_u32_e32 v12, 0, v12
	ds_read_b32 v3, v3 offset:32
	ds_read_b32 v45, v12 offset:32
	v_ashrrev_i32_e32 v59, 31, v14
	v_mov_b32_e32 v58, v14
	s_waitcnt lgkmcnt(2)
	v_lshlrev_b32_e32 v14, 2, v16
	v_add_u32_e32 v14, 0, v14
	s_waitcnt lgkmcnt(1)
	v_add_u32_e32 v12, v13, v3
	v_lshlrev_b64 v[56:57], 25, v[56:57]
	ds_read_b32 v47, v14 offset:32
	s_waitcnt lgkmcnt(1)
	v_add_u32_e32 v14, v15, v45
	v_ashrrev_i32_e32 v13, 31, v12
	v_lshlrev_b64 v[58:59], 25, v[58:59]
	v_lshl_add_u64 v[56:57], s[24:25], 0, v[56:57]
	v_ashrrev_i32_e32 v15, 31, v14
	v_lshlrev_b64 v[12:13], 11, v[12:13]
	v_lshl_add_u64 v[58:59], s[24:25], 0, v[58:59]
	v_lshlrev_b64 v[14:15], 11, v[14:15]
	v_lshl_add_u64 v[12:13], v[56:57], 0, v[12:13]
	v_lshl_add_u64 v[54:55], v[32:33], 0, s[0:1]
	v_lshl_add_u64 v[14:15], v[58:59], 0, v[14:15]
	v_readfirstlane_b32 s0, v12
	v_readfirstlane_b32 s1, v13
	v_readfirstlane_b32 s8, v14
	v_readfirstlane_b32 s9, v15
	v_lshlrev_b32_e32 v3, 2, v18
	v_add_u32_e32 v3, 0, v3
	v_ashrrev_i32_e32 v61, 31, v16
	v_mov_b32_e32 v60, v16
	v_ashrrev_i32_e32 v63, 31, v18
	v_mov_b32_e32 v62, v18
	v_lshlrev_b64 v[60:61], 25, v[60:61]
	v_lshlrev_b64 v[62:63], 25, v[62:63]
	v_lshl_add_u64 v[60:61], s[24:25], 0, v[60:61]
	v_lshl_add_u64 v[62:63], s[24:25], 0, v[62:63]
	s_add_i32 s42, s42, s44
	s_add_i32 s47, s47, s48
	s_add_i32 s49, s49, s44
	s_waitcnt vmcnt(14)
	global_store_dwordx4 v132, v[150:153], s[0:1]
	global_store_dwordx4 v132, v[154:157], s[0:1] offset:1024
	global_store_dwordx4 v132, v[150:153], s[8:9]
	global_store_dwordx4 v132, v[154:157], s[8:9] offset:1024
	s_nop 0
	ds_read_b128 v[12:15], v2 offset:96
	ds_read_b128 v[54:57], v2 offset:112
	ds_read_b32 v3, v3 offset:32
	s_or_b32 s0, s26, 2
	s_ashr_i32 s1, s0, 31
	s_waitcnt lgkmcnt(2)
	v_lshlrev_b32_e32 v16, 2, v12
	v_add_u32_e32 v16, 0, v16
	ds_read_b32 v45, v16 offset:32
	v_add_u32_e32 v16, v17, v47
	s_waitcnt lgkmcnt(1)
	v_add_u32_e32 v18, v19, v3
	v_ashrrev_i32_e32 v17, 31, v16
	v_ashrrev_i32_e32 v19, 31, v18
	v_lshlrev_b64 v[16:17], 11, v[16:17]
	s_lshl_b64 s[0:1], s[0:1], 11
	v_lshlrev_b64 v[18:19], 11, v[18:19]
	v_lshl_add_u64 v[16:17], v[60:61], 0, v[16:17]
	v_lshl_add_u64 v[58:59], v[32:33], 0, s[0:1]
	v_lshl_add_u64 v[18:19], v[62:63], 0, v[18:19]
	v_readfirstlane_b32 s0, v16
	v_readfirstlane_b32 s1, v17
	v_readfirstlane_b32 s8, v18
	v_readfirstlane_b32 s9, v19
	v_lshlrev_b32_e32 v3, 2, v14
	v_add_u32_e32 v3, 0, v3
	v_ashrrev_i32_e32 v19, 31, v12
	v_mov_b32_e32 v18, v12
	v_lshlrev_b32_e32 v12, 2, v54
	v_add_u32_e32 v12, 0, v12
	v_lshlrev_b64 v[18:19], 25, v[18:19]
	v_lshl_add_u64 v[18:19], s[24:25], 0, v[18:19]
	s_waitcnt vmcnt(16)
	global_store_dwordx4 v132, v[158:161], s[0:1]
	global_store_dwordx4 v132, v[162:165], s[0:1] offset:1024
	global_store_dwordx4 v132, v[158:161], s[8:9]
	global_store_dwordx4 v132, v[162:165], s[8:9] offset:1024
	s_nop 0
	ds_read_b32 v3, v3 offset:32
	ds_read_b32 v47, v12 offset:32
	s_waitcnt lgkmcnt(2)
	v_add_u32_e32 v12, v13, v45
	s_or_b32 s0, s26, 3
	v_ashrrev_i32_e32 v59, 31, v14
	v_mov_b32_e32 v58, v14
	s_waitcnt lgkmcnt(1)
	v_add_u32_e32 v14, v15, v3
	v_ashrrev_i32_e32 v13, 31, v12
	s_ashr_i32 s1, s0, 31
	v_lshlrev_b64 v[58:59], 25, v[58:59]
	v_ashrrev_i32_e32 v15, 31, v14
	v_lshlrev_b64 v[12:13], 11, v[12:13]
	s_lshl_b64 s[0:1], s[0:1], 11
	v_lshl_add_u64 v[58:59], s[24:25], 0, v[58:59]
	v_lshlrev_b64 v[14:15], 11, v[14:15]
	v_lshl_add_u64 v[12:13], v[18:19], 0, v[12:13]
	v_lshl_add_u64 v[16:17], v[32:33], 0, s[0:1]
	v_lshl_add_u64 v[14:15], v[58:59], 0, v[14:15]
	v_readfirstlane_b32 s0, v12
	v_readfirstlane_b32 s1, v13
	v_readfirstlane_b32 s8, v14
	v_readfirstlane_b32 s9, v15
	v_lshlrev_b32_e32 v3, 2, v56
	v_add_u32_e32 v3, 0, v3
	v_ashrrev_i32_e32 v15, 31, v54
	v_mov_b32_e32 v14, v54
	s_waitcnt lgkmcnt(0)
; #define GAS __attribute__((address_space(1)))
; #define LAS __attribute__((address_space(3)))
; __device__ __forceinline__ void route_phase(Frame& F) {
;     ...
;         { unsigned char* XGS = F.ws + WS_XGS;
; #pragma unroll
;           for (int i = 0; i < 8; ++i) { const int row = base + F.wave * 8 + i; const LAS int* pr = lrow + (F.wave * 8 + i) * 4;
;               const v4u* src = (const v4u*)((const unsigned char*)XN + (size_t)row * DM) + F.lane;
;               const v4u x0 = __builtin_nontemporal_load((const GAS v4u*)src), x1 = __builtin_nontemporal_load((const GAS v4u*)(src + 64));
; #pragma unroll
;               for (int sl = 0; sl < 2; ++sl) { const int e = pr[2 * sl], rk = lbase[e] + pr[2 * sl + 1];
;                   GAS v4u* dst = (GAS v4u*)(XGS + ((size_t)e * ML + rk) * DM) + F.lane; dst[0] = x0; dst[64] = x1; } } }
	v_add_u32_e32 v18, v55, v47
	v_lshlrev_b64 v[14:15], 25, v[14:15]
	v_ashrrev_i32_e32 v19, 31, v18
	v_lshl_add_u64 v[14:15], s[24:25], 0, v[14:15]
	v_lshlrev_b64 v[18:19], 11, v[18:19]
	v_lshl_add_u64 v[14:15], v[14:15], 0, v[18:19]
	s_waitcnt vmcnt(18)
	global_store_dwordx4 v132, v[166:169], s[0:1]
	global_store_dwordx4 v132, v[170:173], s[0:1] offset:1024
	global_store_dwordx4 v132, v[166:169], s[8:9]
	global_store_dwordx4 v132, v[170:173], s[8:9] offset:1024
	s_nop 0
	ds_read_b32 v3, v3 offset:32
	s_or_b32 s0, s26, 4
	v_ashrrev_i32_e32 v17, 31, v56
	v_mov_b32_e32 v16, v56
	s_ashr_i32 s1, s0, 31
	s_waitcnt lgkmcnt(0)
	v_add_u32_e32 v54, v57, v3
	v_lshlrev_b64 v[16:17], 25, v[16:17]
	v_ashrrev_i32_e32 v55, 31, v54
	s_lshl_b64 s[0:1], s[0:1], 11
	v_lshl_add_u64 v[16:17], s[24:25], 0, v[16:17]
	v_lshlrev_b64 v[54:55], 11, v[54:55]
	v_lshl_add_u64 v[12:13], v[32:33], 0, s[0:1]
	v_lshl_add_u64 v[16:17], v[16:17], 0, v[54:55]
	v_readfirstlane_b32 s0, v14
	v_readfirstlane_b32 s1, v15
	v_readfirstlane_b32 s8, v16
	v_readfirstlane_b32 s9, v17
	s_waitcnt vmcnt(20)
	s_nop 1
	global_store_dwordx4 v132, v[174:177], s[0:1]
	global_store_dwordx4 v132, v[182:185], s[0:1] offset:1024
	global_store_dwordx4 v132, v[174:177], s[8:9]
	global_store_dwordx4 v132, v[182:185], s[8:9] offset:1024
	s_nop 0
	ds_read_b128 v[12:15], v2 offset:128
	ds_read_b128 v[16:19], v2 offset:144
	s_or_b32 s0, s26, 5
	s_ashr_i32 s1, s0, 31
	s_lshl_b64 s[0:1], s[0:1], 11
	s_waitcnt lgkmcnt(1)
	v_lshlrev_b32_e32 v3, 2, v12
	v_ashrrev_i32_e32 v57, 31, v12
	v_mov_b32_e32 v56, v12
	v_lshlrev_b32_e32 v12, 2, v14
	v_add_u32_e32 v3, 0, v3
	v_add_u32_e32 v12, 0, v12
	ds_read_b32 v3, v3 offset:32
	ds_read_b32 v45, v12 offset:32
	v_ashrrev_i32_e32 v59, 31, v14
	v_mov_b32_e32 v58, v14
	s_waitcnt lgkmcnt(2)
	v_lshlrev_b32_e32 v14, 2, v16
	v_add_u32_e32 v14, 0, v14
	s_waitcnt lgkmcnt(1)
	v_add_u32_e32 v12, v13, v3
	v_lshlrev_b64 v[56:57], 25, v[56:57]
	ds_read_b32 v47, v14 offset:32
	s_waitcnt lgkmcnt(1)
	v_add_u32_e32 v14, v15, v45
	v_ashrrev_i32_e32 v13, 31, v12
	v_lshlrev_b64 v[58:59], 25, v[58:59]
	v_lshl_add_u64 v[56:57], s[24:25], 0, v[56:57]
	v_ashrrev_i32_e32 v15, 31, v14
	v_lshlrev_b64 v[12:13], 11, v[12:13]
	v_lshl_add_u64 v[58:59], s[24:25], 0, v[58:59]
	v_lshlrev_b64 v[14:15], 11, v[14:15]
	v_lshl_add_u64 v[12:13], v[56:57], 0, v[12:13]
	v_lshl_add_u64 v[54:55], v[32:33], 0, s[0:1]
	v_lshl_add_u64 v[14:15], v[58:59], 0, v[14:15]
	v_readfirstlane_b32 s0, v12
	v_readfirstlane_b32 s1, v13
	v_readfirstlane_b32 s8, v14
	v_readfirstlane_b32 s9, v15
	v_ashrrev_i32_e32 v3, 31, v16
	v_ashrrev_i32_e32 v61, 31, v18
	v_mov_b32_e32 v60, v18
	v_lshlrev_b64 v[60:61], 25, v[60:61]
	v_lshl_add_u64 v[60:61], s[24:25], 0, v[60:61]
	s_waitcnt vmcnt(22)
	global_store_dwordx4 v132, v[186:189], s[0:1]
	global_store_dwordx4 v132, v[190:193], s[0:1] offset:1024
	global_store_dwordx4 v132, v[186:189], s[8:9]
	global_store_dwordx4 v132, v[190:193], s[8:9] offset:1024
	s_nop 0
	ds_read_b128 v[12:15], v2 offset:160
	ds_read_b128 v[54:57], v2 offset:176
	v_mov_b32_e32 v2, v16
	v_lshlrev_b32_e32 v16, 2, v18
	v_add_u32_e32 v16, 0, v16
	ds_read_b32 v45, v16 offset:32
	s_waitcnt lgkmcnt(2)
	v_lshlrev_b32_e32 v18, 2, v12
	v_add_u32_e32 v18, 0, v18
	ds_read_b32 v49, v18 offset:32
	v_add_u32_e32 v16, v17, v47
	s_or_b32 s0, s26, 6
	v_lshlrev_b64 v[2:3], 25, v[2:3]
	s_waitcnt lgkmcnt(1)
	v_add_u32_e32 v18, v19, v45
	v_ashrrev_i32_e32 v17, 31, v16
	s_ashr_i32 s1, s0, 31
	v_lshl_add_u64 v[2:3], s[24:25], 0, v[2:3]
	v_ashrrev_i32_e32 v19, 31, v18
	v_lshlrev_b64 v[16:17], 11, v[16:17]
	s_lshl_b64 s[0:1], s[0:1], 11
	v_lshlrev_b64 v[18:19], 11, v[18:19]
	v_lshl_add_u64 v[2:3], v[2:3], 0, v[16:17]
	v_lshl_add_u64 v[58:59], v[32:33], 0, s[0:1]
	v_lshl_add_u64 v[16:17], v[60:61], 0, v[18:19]
	v_readfirstlane_b32 s0, v2
	v_readfirstlane_b32 s1, v3
	v_readfirstlane_b32 s8, v16
	v_readfirstlane_b32 s9, v17
	v_ashrrev_i32_e32 v17, 31, v12
	v_mov_b32_e32 v16, v12
	v_lshlrev_b32_e32 v12, 2, v14
	v_add_u32_e32 v12, 0, v12
	v_ashrrev_i32_e32 v19, 31, v14
	v_mov_b32_e32 v18, v14
	v_lshlrev_b32_e32 v14, 2, v54
	v_add_u32_e32 v14, 0, v14
	v_lshlrev_b64 v[16:17], 25, v[16:17]
	v_lshlrev_b64 v[18:19], 25, v[18:19]
	v_lshl_add_u64 v[16:17], s[24:25], 0, v[16:17]
	v_lshl_add_u64 v[18:19], s[24:25], 0, v[18:19]
	s_waitcnt vmcnt(24)
	global_store_dwordx4 v132, v[194:197], s[0:1]
	global_store_dwordx4 v132, v[200:203], s[0:1] offset:1024
	global_store_dwordx4 v132, v[194:197], s[8:9]
	global_store_dwordx4 v132, v[200:203], s[8:9] offset:1024
	s_nop 0
	ds_read_b32 v45, v12 offset:32
	ds_read_b32 v47, v14 offset:32
	s_waitcnt lgkmcnt(2)
	v_add_u32_e32 v12, v13, v49
	s_or_b32 s0, s26, 7
	v_ashrrev_i32_e32 v13, 31, v12
	s_waitcnt lgkmcnt(1)
	v_add_u32_e32 v14, v15, v45
	s_ashr_i32 s1, s0, 31
	v_ashrrev_i32_e32 v15, 31, v14
	v_lshlrev_b64 v[12:13], 11, v[12:13]
	s_lshl_b64 s[0:1], s[0:1], 11
	v_lshlrev_b64 v[14:15], 11, v[14:15]
	v_lshl_add_u64 v[12:13], v[16:17], 0, v[12:13]
	v_lshl_add_u64 v[10:11], v[32:33], 0, s[0:1]
	v_lshl_add_u64 v[14:15], v[18:19], 0, v[14:15]
	v_readfirstlane_b32 s0, v12
	v_readfirstlane_b32 s1, v13
	v_readfirstlane_b32 s8, v14
	v_readfirstlane_b32 s9, v15
	v_lshlrev_b32_e32 v14, 2, v56
	v_add_u32_e32 v14, 0, v14
	v_ashrrev_i32_e32 v13, 31, v56
	v_mov_b32_e32 v12, v56
	v_lshlrev_b64 v[12:13], 25, v[12:13]
	v_lshl_add_u64 v[12:13], s[24:25], 0, v[12:13]
	s_cmpk_lt_i32 s42, 0x4000
	s_waitcnt vmcnt(26)
	global_store_dwordx4 v132, v[204:207], s[0:1]
	global_store_dwordx4 v132, v[208:211], s[0:1] offset:1024
	global_store_dwordx4 v132, v[204:207], s[8:9]
	global_store_dwordx4 v132, v[208:211], s[8:9] offset:1024
	s_nop 0
	ds_read_b32 v15, v14 offset:32
	v_ashrrev_i32_e32 v11, 31, v54
	v_mov_b32_e32 v10, v54
	s_waitcnt lgkmcnt(1)
	v_add_u32_e32 v14, v55, v47
	v_lshlrev_b64 v[10:11], 25, v[10:11]
	s_waitcnt lgkmcnt(0)
	v_add_u32_e32 v16, v57, v15
	v_ashrrev_i32_e32 v15, 31, v14
	v_lshl_add_u64 v[10:11], s[24:25], 0, v[10:11]
	v_ashrrev_i32_e32 v17, 31, v16
	v_lshlrev_b64 v[14:15], 11, v[14:15]
	v_lshlrev_b64 v[16:17], 11, v[16:17]
	v_lshl_add_u64 v[10:11], v[10:11], 0, v[14:15]
	v_lshl_add_u64 v[12:13], v[12:13], 0, v[16:17]
	v_readfirstlane_b32 s0, v10
	v_readfirstlane_b32 s1, v11
	v_readfirstlane_b32 s8, v12
	v_readfirstlane_b32 s9, v13
	s_waitcnt vmcnt(28)
	s_nop 1
	global_store_dwordx4 v132, v[212:215], s[0:1]
	global_store_dwordx4 v132, v[216:219], s[0:1] offset:1024
	global_store_dwordx4 v132, v[212:215], s[8:9]
	global_store_dwordx4 v132, v[216:219], s[8:9] offset:1024
	s_cbranch_scc0 .LBB0_1752
